# loop-head alignment to 64B for GEMM K-loops, DSA and indexer loops + relaxed false vmcnt waits in DSA steps
# speedup vs baseline: 1.2522x; 1.2522x over previous
.LBB0_97:
	s_add_u32 s95, s52, 0x100
	s_addc_u32 s46, s53, 0
	s_add_u32 s52, s50, 0xb0080
	s_addc_u32 s53, s51, 0
	v_lshl_add_u64 v[140:141], s[52:53], 0, v[136:137]
	v_lshl_add_u64 v[142:143], s[52:53], 0, v[138:139]
	s_mov_b32 s47, -2
	s_mov_b64 s[52:53], 0
	.p2align	6

.LBB0_356:
	s_ashr_i32 s57, s56, 31
	s_lshl_b64 s[60:61], s[56:57], 19
	v_readlane_b32 s29, v253, 49
	s_add_u32 s60, s29, s60
	v_readlane_b32 s29, v253, 50
	s_addc_u32 s61, s29, s61
	s_and_b64 s[64:65], s[62:63], exec
	s_cselect_b32 s29, s61, s41
	s_cselect_b32 s37, s60, s40
	s_ashr_i32 s59, s58, 31
	s_lshl_b64 s[64:65], s[58:59], 19
	v_readlane_b32 s39, v253, 52
	s_add_u32 s64, s39, s64
	v_readlane_b32 s39, v253, 53
	s_addc_u32 s65, s39, s65
	s_and_b64 s[82:83], s[62:63], exec
	s_cselect_b32 s39, s65, s67
	s_cselect_b32 s57, s64, s66
	s_add_u32 s40, s40, 0x40080
	s_addc_u32 s41, s41, 0
	s_add_u32 s59, s66, 0x100
	v_mov_b32_e32 v2, 0
	s_addc_u32 vcc_lo, s67, 0
	s_mov_b32 vcc_hi, -2
	v_mov_b32_e32 v3, v2
	v_mov_b32_e32 v4, v2
	v_mov_b32_e32 v5, v2
	v_mov_b32_e32 v6, v2
	v_mov_b32_e32 v7, v2
	v_mov_b32_e32 v8, v2
	v_mov_b32_e32 v9, v2
	v_mov_b32_e32 v18, v2
	v_mov_b32_e32 v19, v2
	v_mov_b32_e32 v20, v2
	v_mov_b32_e32 v21, v2
	v_mov_b32_e32 v22, v2
	v_mov_b32_e32 v23, v2
	v_mov_b32_e32 v24, v2
	v_mov_b32_e32 v25, v2
	v_mov_b32_e32 v34, v2
	v_mov_b32_e32 v35, v2
	v_mov_b32_e32 v36, v2
	v_mov_b32_e32 v37, v2
	v_mov_b32_e32 v38, v2
	v_mov_b32_e32 v39, v2
	v_mov_b32_e32 v40, v2
	v_mov_b32_e32 v41, v2
	v_mov_b32_e32 v66, v2
	v_mov_b32_e32 v67, v2
	v_mov_b32_e32 v68, v2
	v_mov_b32_e32 v69, v2
	v_mov_b32_e32 v70, v2
	v_mov_b32_e32 v71, v2
	v_mov_b32_e32 v72, v2
	v_mov_b32_e32 v73, v2
	v_mov_b32_e32 v10, v2
	v_mov_b32_e32 v11, v2
	v_mov_b32_e32 v12, v2
	v_mov_b32_e32 v13, v2
	v_mov_b32_e32 v14, v2
	v_mov_b32_e32 v15, v2
	v_mov_b32_e32 v16, v2
	v_mov_b32_e32 v17, v2
	v_mov_b32_e32 v26, v2
	v_mov_b32_e32 v27, v2
	v_mov_b32_e32 v28, v2
	v_mov_b32_e32 v29, v2
	v_mov_b32_e32 v30, v2
	v_mov_b32_e32 v31, v2
	v_mov_b32_e32 v32, v2
	v_mov_b32_e32 v33, v2
	v_mov_b32_e32 v42, v2
	v_mov_b32_e32 v43, v2
	v_mov_b32_e32 v44, v2
	v_mov_b32_e32 v45, v2
	v_mov_b32_e32 v54, v2
	v_mov_b32_e32 v55, v2
	v_mov_b32_e32 v56, v2
	v_mov_b32_e32 v57, v2
	v_mov_b32_e32 v90, v2
	v_mov_b32_e32 v91, v2
	v_mov_b32_e32 v92, v2
	v_mov_b32_e32 v93, v2
	v_mov_b32_e32 v94, v2
	v_mov_b32_e32 v95, v2
	v_mov_b32_e32 v96, v2
	v_mov_b32_e32 v97, v2
	v_mov_b32_e32 v98, v2
	v_mov_b32_e32 v99, v2
	v_mov_b32_e32 v100, v2
	v_mov_b32_e32 v101, v2
	v_mov_b32_e32 v102, v2
	v_mov_b32_e32 v103, v2
	v_mov_b32_e32 v104, v2
	v_mov_b32_e32 v105, v2
	v_mov_b32_e32 v114, v2
	v_mov_b32_e32 v115, v2
	v_mov_b32_e32 v116, v2
	v_mov_b32_e32 v117, v2
	v_mov_b32_e32 v118, v2
	v_mov_b32_e32 v119, v2
	v_mov_b32_e32 v120, v2
	v_mov_b32_e32 v121, v2
	v_mov_b32_e32 v130, v2
	v_mov_b32_e32 v131, v2
	v_mov_b32_e32 v132, v2
	v_mov_b32_e32 v133, v2
	v_mov_b32_e32 v134, v2
	v_mov_b32_e32 v135, v2
	v_mov_b32_e32 v136, v2
	v_mov_b32_e32 v137, v2
	v_mov_b32_e32 v146, v2
	v_mov_b32_e32 v147, v2
	v_mov_b32_e32 v148, v2
	v_mov_b32_e32 v149, v2
	v_mov_b32_e32 v150, v2
	v_mov_b32_e32 v151, v2
	v_mov_b32_e32 v152, v2
	v_mov_b32_e32 v153, v2
	v_mov_b32_e32 v106, v2
	v_mov_b32_e32 v107, v2
	v_mov_b32_e32 v108, v2
	v_mov_b32_e32 v109, v2
	v_mov_b32_e32 v110, v2
	v_mov_b32_e32 v111, v2
	v_mov_b32_e32 v112, v2
	v_mov_b32_e32 v113, v2
	v_mov_b32_e32 v122, v2
	v_mov_b32_e32 v123, v2
	v_mov_b32_e32 v124, v2
	v_mov_b32_e32 v125, v2
	v_mov_b32_e32 v126, v2
	v_mov_b32_e32 v127, v2
	v_mov_b32_e32 v128, v2
	v_mov_b32_e32 v129, v2
	v_mov_b32_e32 v138, v2
	v_mov_b32_e32 v139, v2
	v_mov_b32_e32 v140, v2
	v_mov_b32_e32 v141, v2
	v_mov_b32_e32 v142, v2
	v_mov_b32_e32 v143, v2
	v_mov_b32_e32 v144, v2
	v_mov_b32_e32 v145, v2
	v_mov_b32_e32 v154, v2
	v_mov_b32_e32 v155, v2
	v_mov_b32_e32 v156, v2
	v_mov_b32_e32 v157, v2
	v_mov_b32_e32 v158, v2
	v_mov_b32_e32 v159, v2
	v_mov_b32_e32 v160, v2
	v_mov_b32_e32 v161, v2
	.p2align	6

.LBB0_396:
	s_ashr_i32 s39, s38, 31
	s_lshl_b64 s[46:47], s[38:39], 19
	s_add_u32 s46, s17, s46
	s_addc_u32 s47, s34, s47
	s_and_b64 s[52:53], s[52:53], exec
	s_cselect_b32 s90, s47, s49
	s_cselect_b32 s91, s46, s48
	s_add_u32 s39, s50, 0x100
	s_addc_u32 s41, s51, 0
	s_add_u32 s50, s48, 0x40080
	s_addc_u32 s51, s49, 0
	v_lshl_add_u64 v[140:141], s[50:51], 0, v[136:137]
	v_lshl_add_u64 v[142:143], s[50:51], 0, v[138:139]
	s_mov_b32 s92, -2
	s_mov_b64 s[50:51], 0
	.p2align	6

.LBB0_437:
	s_ashr_i32 s39, s38, 31
	s_lshl_b64 s[46:47], s[38:39], 19
	s_add_u32 s46, s54, s46
	s_addc_u32 s47, s55, s47
	s_and_b64 s[50:51], s[50:51], exec
	s_cselect_b32 s29, s47, s17
	s_cselect_b32 s39, s46, s16
	s_add_u32 s41, s48, 0x100
	s_addc_u32 s89, s49, 0
	s_add_u32 s48, s16, 0x40080
	s_addc_u32 s49, s17, 0
	v_lshl_add_u64 v[156:157], s[48:49], 0, v[152:153]
	v_lshl_add_u64 v[158:159], s[48:49], 0, v[154:155]
	s_mov_b32 s90, -2
	s_mov_b64 s[48:49], 0
	.p2align	6

.LBB0_495:
	s_add_u32 s92, s52, 0x100
	s_addc_u32 s93, s53, 0
	s_ashr_i32 s39, s38, 31
	s_lshl_b64 s[44:45], s[38:39], 19
	s_add_u32 s44, s31, s44
	s_addc_u32 s45, s34, s45
	s_and_b64 s[46:47], s[50:51], exec
	s_cselect_b32 s39, s45, s49
	s_cselect_b32 s94, s44, s48
	s_ashr_i32 s41, s40, 31
	s_lshl_b64 s[46:47], s[40:41], 19
	s_add_u32 s46, s35, s46
	s_addc_u32 s47, s58, s47
	s_and_b64 s[54:55], s[50:51], exec
	s_cselect_b32 s41, s47, s53
	s_cselect_b32 s95, s46, s52
	s_add_u32 s52, s48, 0x40080
	s_addc_u32 s53, s49, 0
	v_lshl_add_u64 v[140:141], s[52:53], 0, v[136:137]
	v_lshl_add_u64 v[142:143], s[52:53], 0, v[138:139]
	s_mov_b32 vcc_lo, -2
	s_mov_b64 s[52:53], 0
	.p2align	6

.LBB0_534:
	s_add_u32 s29, s52, 0x100
	s_addc_u32 s93, s53, 0
	s_ashr_i32 s39, s38, 31
	s_lshl_b64 s[46:47], s[38:39], 19
	s_add_u32 s46, s31, s46
	s_addc_u32 s47, s34, s47
	s_and_b64 s[48:49], s[50:51], exec
	s_cselect_b32 s39, s47, s43
	s_cselect_b32 s94, s46, s42
	s_ashr_i32 s41, s40, 31
	s_lshl_b64 s[48:49], s[40:41], 19
	s_add_u32 s48, s35, s48
	s_addc_u32 s49, s58, s49
	s_and_b64 s[54:55], s[50:51], exec
	s_cselect_b32 s41, s49, s53
	s_cselect_b32 s95, s48, s52
	s_add_u32 s52, s42, 0x40080
	s_addc_u32 s53, s43, 0
	v_lshl_add_u64 v[140:141], s[52:53], 0, v[136:137]
	v_lshl_add_u64 v[142:143], s[52:53], 0, v[138:139]
	s_mov_b32 vcc_lo, -2
	s_mov_b64 s[52:53], 0
	.p2align	6

.LBB0_850:
	s_add_u32 s54, s54, 0x20080
	s_addc_u32 s55, s55, 0
	s_add_u32 s29, s56, 0x100
	s_addc_u32 s39, s57, 0
	s_mov_b32 s41, -2
	.p2align	6

.LBB0_1057:
	s_ashr_i32 s39, s38, 31
	s_lshl_b64 s[42:43], s[38:39], 19
	v_readlane_b32 s44, v253, 34
	v_readlane_b32 s45, v253, 35
	s_add_u32 s42, s44, s42
	s_addc_u32 s43, s45, s43
	s_and_b64 s[44:45], s[46:47], exec
	s_cselect_b32 s29, s43, s37
	s_cselect_b32 s39, s42, s36
	s_ashr_i32 s41, s40, 31
	s_lshl_b64 s[44:45], s[40:41], 19
	s_add_u32 s44, s31, s44
	s_addc_u32 s45, s34, s45
	s_and_b64 s[50:51], s[46:47], exec
	s_cselect_b32 s41, s45, s49
	s_cselect_b32 s85, s44, s48
	s_add_u32 s36, s36, 0x40080
	s_addc_u32 s37, s37, 0
	s_add_u32 s88, s48, 0x100
	v_mov_b32_e32 v2, 0
	s_addc_u32 s89, s49, 0
	s_mov_b32 s90, -2
	v_mov_b32_e32 v3, v2
	v_mov_b32_e32 v4, v2
	v_mov_b32_e32 v5, v2
	v_mov_b32_e32 v6, v2
	v_mov_b32_e32 v7, v2
	v_mov_b32_e32 v8, v2
	v_mov_b32_e32 v9, v2
	v_mov_b32_e32 v18, v2
	v_mov_b32_e32 v19, v2
	v_mov_b32_e32 v20, v2
	v_mov_b32_e32 v21, v2
	v_mov_b32_e32 v22, v2
	v_mov_b32_e32 v23, v2
	v_mov_b32_e32 v24, v2
	v_mov_b32_e32 v25, v2
	v_mov_b32_e32 v34, v2
	v_mov_b32_e32 v35, v2
	v_mov_b32_e32 v36, v2
	v_mov_b32_e32 v37, v2
	v_mov_b32_e32 v38, v2
	v_mov_b32_e32 v39, v2
	v_mov_b32_e32 v40, v2
	v_mov_b32_e32 v41, v2
	v_mov_b32_e32 v50, v2
	v_mov_b32_e32 v51, v2
	v_mov_b32_e32 v52, v2
	v_mov_b32_e32 v53, v2
	v_mov_b32_e32 v54, v2
	v_mov_b32_e32 v55, v2
	v_mov_b32_e32 v56, v2
	v_mov_b32_e32 v57, v2
	v_mov_b32_e32 v10, v2
	v_mov_b32_e32 v11, v2
	v_mov_b32_e32 v12, v2
	v_mov_b32_e32 v13, v2
	v_mov_b32_e32 v14, v2
	v_mov_b32_e32 v15, v2
	v_mov_b32_e32 v16, v2
	v_mov_b32_e32 v17, v2
	v_mov_b32_e32 v26, v2
	v_mov_b32_e32 v27, v2
	v_mov_b32_e32 v28, v2
	v_mov_b32_e32 v29, v2
	v_mov_b32_e32 v30, v2
	v_mov_b32_e32 v31, v2
	v_mov_b32_e32 v32, v2
	v_mov_b32_e32 v33, v2
	v_mov_b32_e32 v42, v2
	v_mov_b32_e32 v43, v2
	v_mov_b32_e32 v44, v2
	v_mov_b32_e32 v45, v2
	v_mov_b32_e32 v46, v2
	v_mov_b32_e32 v47, v2
	v_mov_b32_e32 v48, v2
	v_mov_b32_e32 v49, v2
	v_mov_b32_e32 v58, v2
	v_mov_b32_e32 v59, v2
	v_mov_b32_e32 v60, v2
	v_mov_b32_e32 v61, v2
	v_mov_b32_e32 v62, v2
	v_mov_b32_e32 v63, v2
	v_mov_b32_e32 v64, v2
	v_mov_b32_e32 v65, v2
	v_mov_b32_e32 v66, v2
	v_mov_b32_e32 v67, v2
	v_mov_b32_e32 v68, v2
	v_mov_b32_e32 v69, v2
	v_mov_b32_e32 v70, v2
	v_mov_b32_e32 v71, v2
	v_mov_b32_e32 v72, v2
	v_mov_b32_e32 v73, v2
	v_mov_b32_e32 v82, v2
	v_mov_b32_e32 v83, v2
	v_mov_b32_e32 v84, v2
	v_mov_b32_e32 v85, v2
	v_mov_b32_e32 v86, v2
	v_mov_b32_e32 v87, v2
	v_mov_b32_e32 v88, v2
	v_mov_b32_e32 v89, v2
	v_mov_b32_e32 v98, v2
	v_mov_b32_e32 v99, v2
	v_mov_b32_e32 v100, v2
	v_mov_b32_e32 v101, v2
	v_mov_b32_e32 v102, v2
	v_mov_b32_e32 v103, v2
	v_mov_b32_e32 v104, v2
	v_mov_b32_e32 v105, v2
	v_mov_b32_e32 v114, v2
	v_mov_b32_e32 v115, v2
	v_mov_b32_e32 v116, v2
	v_mov_b32_e32 v117, v2
	v_mov_b32_e32 v118, v2
	v_mov_b32_e32 v119, v2
	v_mov_b32_e32 v120, v2
	v_mov_b32_e32 v121, v2
	v_mov_b32_e32 v74, v2
	v_mov_b32_e32 v75, v2
	v_mov_b32_e32 v76, v2
	v_mov_b32_e32 v77, v2
	v_mov_b32_e32 v78, v2
	v_mov_b32_e32 v79, v2
	v_mov_b32_e32 v80, v2
	v_mov_b32_e32 v81, v2
	v_mov_b32_e32 v90, v2
	v_mov_b32_e32 v91, v2
	v_mov_b32_e32 v92, v2
	v_mov_b32_e32 v93, v2
	v_mov_b32_e32 v94, v2
	v_mov_b32_e32 v95, v2
	v_mov_b32_e32 v96, v2
	v_mov_b32_e32 v97, v2
	v_mov_b32_e32 v106, v2
	v_mov_b32_e32 v107, v2
	v_mov_b32_e32 v108, v2
	v_mov_b32_e32 v109, v2
	v_mov_b32_e32 v110, v2
	v_mov_b32_e32 v111, v2
	v_mov_b32_e32 v112, v2
	v_mov_b32_e32 v113, v2
	v_mov_b32_e32 v122, v2
	v_mov_b32_e32 v123, v2
	v_mov_b32_e32 v124, v2
	v_mov_b32_e32 v125, v2
	v_mov_b32_e32 v126, v2
	v_mov_b32_e32 v127, v2
	v_mov_b32_e32 v128, v2
	v_mov_b32_e32 v129, v2
	.p2align	6

.LBB0_1075:
	s_waitcnt vmcnt(0) lgkmcnt(0)
	s_barrier
	v_exp_f32_e32 v48, v2
	v_exp_f32_e32 v49, v3
	v_lshl_add_u64 v[2:3], v[216:217], 0, s[70:71]
	s_mov_b32 s38, m0
	s_mov_b32 m0, s63
	s_nop 0
	global_load_lds_dwordx4 v[2:3], off
	s_mov_b32 m0, s38
	v_lshl_add_u64 v[2:3], v[218:219], 0, s[12:13]
	s_add_i32 s38, s63, 0x8000
	s_mov_b32 s39, m0
	s_mov_b32 m0, s38
	s_nop 0
	global_load_lds_dwordx4 v[2:3], off
	s_mov_b32 m0, s39
	ds_read_b128 v[172:175], v241 offset:8192
	ds_read_b128 v[164:167], v241 offset:8704
	ds_read_b128 v[168:171], v241 offset:10240
	ds_read_b128 v[160:163], v241 offset:10752
	ds_read_b128 v[156:159], v241 offset:12288
	ds_read_b128 v[152:155], v241 offset:12800
	ds_read_b128 v[148:151], v241 offset:14336
	ds_read_b128 v[144:147], v241 offset:14848
	v_exp_f32_e32 v64, v37
	v_exp_f32_e32 v65, v18
	v_exp_f32_e32 v66, v19
	v_exp_f32_e32 v67, v20
	v_exp_f32_e32 v68, v21
	v_exp_f32_e32 v69, v22
	v_exp_f32_e32 v70, v23
	v_exp_f32_e32 v71, v24
	v_exp_f32_e32 v72, v25
	v_exp_f32_e32 v73, v26
	v_exp_f32_e32 v74, v27
	v_exp_f32_e32 v75, v28
	v_exp_f32_e32 v76, v29
	v_exp_f32_e32 v77, v30
	v_exp_f32_e32 v78, v31
	v_exp_f32_e32 v79, v32
	v_exp_f32_e32 v50, v4
	v_exp_f32_e32 v51, v5
	v_exp_f32_e32 v52, v6
	v_exp_f32_e32 v53, v7
	v_exp_f32_e32 v54, v8
	v_exp_f32_e32 v55, v9
	v_exp_f32_e32 v56, v10
	v_exp_f32_e32 v57, v11
	v_exp_f32_e32 v58, v12
	v_exp_f32_e32 v59, v13
	v_exp_f32_e32 v60, v14
	v_exp_f32_e32 v61, v15
	v_exp_f32_e32 v62, v16
	v_exp_f32_e32 v63, v17
	s_and_b32 s29, s41, 0x3fffffc0
	s_addk_i32 s42, 0x100
	s_waitcnt vmcnt(2) lgkmcnt(0)
	s_barrier
	s_lshl_b32 s29, s29, 2
	s_lshr_b32 s64, s42, 6
	v_or_b32_e32 v0, v36, v0
	v_cmp_ne_u32_e64 s[42:43], 0, v0
	s_cmp_eq_u32 s40, 0
	v_lshl_add_u32 v205, v236, 2, s29
	v_lshl_add_u32 v203, v238, 2, s29
	v_lshl_add_u64 v[220:221], v[34:35], 2, s[48:49]
	s_cbranch_scc1 .LBB0_1151
	v_mov_b32_e32 v14, v1
	v_mov_b32_e32 v15, v1
	v_lshl_add_u64 v[184:185], v[34:35], 2, s[48:49]
	v_mov_b32_e32 v0, v1
	v_mov_b32_e32 v2, v1
	v_mov_b32_e32 v3, v1
	v_mov_b32_e32 v4, v1
	v_mov_b32_e32 v5, v1
	v_mov_b32_e32 v6, v1
	v_mov_b32_e32 v7, v1
	v_mov_b32_e32 v8, v1
	v_mov_b32_e32 v9, v1
	v_mov_b32_e32 v10, v1
	v_mov_b32_e32 v11, v1
	v_mov_b32_e32 v12, v1
	v_mov_b32_e32 v13, v1
	v_mov_b64_e32 v[46:47], v[14:15]
	v_mov_b64_e32 v[30:31], v[14:15]
	v_lshl_add_u64 v[182:183], v[180:181], 2, s[46:47]
	s_mov_b32 s29, 0
	s_movk_i32 s57, 0x4000
	s_movk_i32 s59, 0x2000
	v_mov_b32_e32 v248, 0
	s_mov_b32 s58, 6
	s_mov_b64 s[54:55], 0
	v_mov_b64_e32 v[44:45], v[12:13]
	v_mov_b64_e32 v[42:43], v[10:11]
	v_mov_b64_e32 v[40:41], v[8:9]
	v_mov_b64_e32 v[38:39], v[6:7]
	v_mov_b64_e32 v[36:37], v[4:5]
	v_mov_b64_e32 v[34:35], v[2:3]
	v_mov_b64_e32 v[32:33], v[0:1]
	v_mov_b64_e32 v[28:29], v[12:13]
	v_mov_b64_e32 v[26:27], v[10:11]
	v_mov_b64_e32 v[24:25], v[8:9]
	v_mov_b64_e32 v[22:23], v[6:7]
	v_mov_b64_e32 v[20:21], v[4:5]
	v_mov_b64_e32 v[18:19], v[2:3]
	v_mov_b64_e32 v[16:17], v[0:1]
	.p2align	6
.LBB0_1077:
	v_lshl_add_u64 v[14:15], v[184:185], 0, s[54:55]
	s_mov_b32 s38, 0xeb20000
	v_add_co_u32_e32 v2, vcc, s38, v14
	s_mov_b32 s38, 0xeb28000
	s_nop 0
	v_addc_co_u32_e32 v3, vcc, 0, v15, vcc
	v_add_co_u32_e32 v4, vcc, s38, v14
	v_add_u32_e32 v12, s29, v239
	s_nop 0
	v_addc_co_u32_e32 v5, vcc, 0, v15, vcc
	global_load_dword v0, v[2:3], off
	global_load_dword v190, v[4:5], off
	global_load_dword v191, v[182:183], off offset:-4
	ds_read_b64_tr_b16 v[176:177], v12 offset:24576
	ds_read_b64_tr_b16 v[178:179], v12 offset:25088
	s_waitcnt lgkmcnt(9)
	v_mfma_f32_32x32x16_bf16 v[80:95], v[172:175], v[124:127], 0
	v_add_f32_e32 v2, v64, v65
	v_add_f32_e32 v2, v66, v2
	v_add_f32_e32 v2, v67, v2
	v_add_f32_e32 v2, v68, v2
	v_add_f32_e32 v2, v69, v2
	v_cvt_pk_bf16_f32 v140, v64, v65
	v_cvt_pk_bf16_f32 v141, v66, v67
	ds_read_b64_tr_b16 v[172:173], v12 offset:28672
	ds_read_b64_tr_b16 v[174:175], v12 offset:29184
	s_waitcnt lgkmcnt(10)
	v_mfma_f32_32x32x16_bf16 v[96:111], v[164:167], v[124:127], 0
	v_add_f32_e32 v2, v70, v2
	v_add_f32_e32 v2, v71, v2
	v_add_f32_e32 v2, v72, v2
	v_add_f32_e32 v2, v73, v2
	v_cvt_pk_bf16_f32 v142, v68, v69
	v_cvt_pk_bf16_f32 v143, v70, v71
	ds_read_b64_tr_b16 v[164:165], v12 offset:25600
	ds_read_b64_tr_b16 v[166:167], v12 offset:26112
	s_waitcnt lgkmcnt(11)
	v_mfma_f32_32x32x16_bf16 v[80:95], v[168:171], v[120:123], v[80:95]
	v_add_f32_e32 v2, v74, v2
	v_add_f32_e32 v2, v75, v2
	v_add_f32_e32 v2, v76, v2
	v_add_f32_e32 v2, v77, v2
	v_cvt_pk_bf16_f32 v136, v72, v73
	v_cvt_pk_bf16_f32 v137, v74, v75
	ds_read_b64_tr_b16 v[168:169], v12 offset:29696
	ds_read_b64_tr_b16 v[170:171], v12 offset:30208
	s_waitcnt lgkmcnt(12)
	v_mfma_f32_32x32x16_bf16 v[96:111], v[160:163], v[120:123], v[96:111]
	v_add_f32_e32 v2, v78, v2
	v_add_f32_e32 v2, v79, v2
	v_add_f32_e32 v2, v48, v2
	v_add_f32_e32 v2, v49, v2
	v_cvt_pk_bf16_f32 v138, v76, v77
	v_cvt_pk_bf16_f32 v139, v78, v79
	ds_read_b64_tr_b16 v[160:161], v12 offset:26624
	ds_read_b64_tr_b16 v[162:163], v12 offset:27136
	s_waitcnt lgkmcnt(13)
	v_mfma_f32_32x32x16_bf16 v[80:95], v[156:159], v[116:119], v[80:95]
	v_add_f32_e32 v2, v50, v2
	v_add_f32_e32 v2, v51, v2
	v_add_f32_e32 v2, v52, v2
	v_add_f32_e32 v6, v53, v2
	v_cvt_pk_bf16_f32 v132, v48, v49
	v_cvt_pk_bf16_f32 v133, v50, v51
	ds_read_b64_tr_b16 v[2:3], v12 offset:30720
	ds_read_b64_tr_b16 v[4:5], v12 offset:31232
	s_waitcnt lgkmcnt(14)
	v_mfma_f32_32x32x16_bf16 v[96:111], v[152:155], v[116:119], v[96:111]
	v_add_f32_e32 v6, v54, v6
	v_add_f32_e32 v6, v55, v6
	v_add_f32_e32 v6, v56, v6
	v_add_f32_e32 v10, v57, v6
	v_cvt_pk_bf16_f32 v134, v52, v53
	v_cvt_pk_bf16_f32 v135, v54, v55
	ds_read_b64_tr_b16 v[6:7], v12 offset:27648
	ds_read_b64_tr_b16 v[8:9], v12 offset:28160
	s_waitcnt lgkmcnt(14)
	v_mfma_f32_32x32x16_bf16 v[80:95], v[148:151], v[112:115], v[80:95]
	v_add_f32_e32 v10, v58, v10
	v_add_f32_e32 v10, v59, v10
	v_add_f32_e32 v10, v60, v10
	v_add_f32_e32 v48, v61, v10
	v_cvt_pk_bf16_f32 v128, v56, v57
	v_cvt_pk_bf16_f32 v129, v58, v59
	ds_read_b64_tr_b16 v[10:11], v12 offset:31744
	ds_read_b64_tr_b16 v[12:13], v12 offset:32256
	v_mfma_f32_32x32x16_bf16 v[96:111], v[144:147], v[112:115], v[96:111]
	v_add_f32_e32 v48, v62, v48
	v_add_f32_e32 v48, v63, v48
	v_add_f32_e32 v48, 0, v48
	v_cvt_pk_bf16_f32 v130, v60, v61
	v_cvt_pk_bf16_f32 v131, v62, v63
	v_lshl_add_u64 v[186:187], v[216:217], 0, s[54:55]
	v_lshl_add_u64 v[50:51], v[186:187], 0, s[20:21]
	s_add_i32 s29, s59, s63
	s_mov_b32 s38, m0
	s_mov_b32 m0, s29
	s_nop 0
	global_load_lds_dwordx4 v[50:51], off
	s_mov_b32 m0, s38
	v_lshl_add_u64 v[188:189], v[218:219], 0, s[54:55]
	v_lshl_add_u64 v[50:51], v[188:189], 0, s[24:25]
	s_add_i32 s29, s57, s62
	s_mov_b32 s38, m0
	s_mov_b32 m0, s29
	s_nop 0
	global_load_lds_dwordx4 v[50:51], off
	s_mov_b32 m0, s38
	s_waitcnt vmcnt(7)
	v_mul_f32_e32 v49, v201, v209
	v_cmp_nge_f32_e32 vcc, s73, v49
	v_cmp_neq_f32_e64 s[38:39], 0, v207
	s_or_b64 vcc, vcc, s[38:39]
	v_cndmask_b32_e64 v49, 0, 1, vcc
	v_cmp_ne_u32_e64 s[38:39], 0, v49
	s_cmp_lg_u64 s[38:39], 0
	s_cselect_b64 s[38:39], -1, 0
	s_cbranch_vccz .LBB0_1079
	v_sub_f32_e32 v95, v95, v207
	v_sub_f32_e32 v94, v94, v207
	v_sub_f32_e32 v93, v93, v207
	v_sub_f32_e32 v92, v92, v207
	v_sub_f32_e32 v91, v91, v207
	v_sub_f32_e32 v90, v90, v207
	v_sub_f32_e32 v89, v89, v207
	v_sub_f32_e32 v88, v88, v207
	v_sub_f32_e32 v87, v87, v207
	v_sub_f32_e32 v86, v86, v207
	v_sub_f32_e32 v85, v85, v207
	v_sub_f32_e32 v84, v84, v207
	v_sub_f32_e32 v83, v83, v207
	v_sub_f32_e32 v82, v82, v207
	v_sub_f32_e32 v81, v81, v207
	v_sub_f32_e32 v80, v80, v207
	v_sub_f32_e32 v111, v111, v207
	v_sub_f32_e32 v110, v110, v207
	v_sub_f32_e32 v109, v109, v207
	v_sub_f32_e32 v108, v108, v207
	v_sub_f32_e32 v107, v107, v207
	v_sub_f32_e32 v106, v106, v207
	v_sub_f32_e32 v105, v105, v207
	v_sub_f32_e32 v104, v104, v207
	v_sub_f32_e32 v103, v103, v207
	v_sub_f32_e32 v102, v102, v207
	v_sub_f32_e32 v101, v101, v207
	v_sub_f32_e32 v100, v100, v207
	v_sub_f32_e32 v99, v99, v207
	v_sub_f32_e32 v98, v98, v207
	v_sub_f32_e32 v97, v97, v207
	v_sub_f32_e32 v96, v96, v207

.LBB0_1082:
	s_add_i32 s29, s57, 0x2000
	s_cmpk_lg_i32 s57, 0x4000
	s_cselect_b32 s65, s29, 0
	v_add_co_u32_e32 v2, vcc, 0xeb30000, v14
	v_add_u32_e32 v12, s59, v239
	s_nop 0
	v_addc_co_u32_e32 v3, vcc, 0, v15, vcc
	global_load_dword v192, v[2:3], off
	v_add_co_u32_e32 v2, vcc, 0xeb38000, v14
	s_nop 1
	v_addc_co_u32_e32 v3, vcc, 0, v15, vcc
	global_load_dword v14, v[2:3], off
	global_load_dword v209, v[182:183], off
	ds_read_b64_tr_b16 v[156:157], v12 offset:24576
	ds_read_b64_tr_b16 v[158:159], v12 offset:25088
	s_waitcnt lgkmcnt(9)
	v_mfma_f32_32x32x16_bf16 v[80:95], v[80:83], v[124:127], 0
	v_add_f32_e32 v2, v64, v65
	v_add_f32_e32 v2, v66, v2
	v_add_f32_e32 v2, v67, v2
	v_add_f32_e32 v2, v68, v2
	v_add_f32_e32 v2, v69, v2
	v_cvt_pk_bf16_f32 v140, v64, v65
	v_cvt_pk_bf16_f32 v141, v66, v67
	ds_read_b64_tr_b16 v[152:153], v12 offset:28672
	ds_read_b64_tr_b16 v[154:155], v12 offset:29184
	s_waitcnt lgkmcnt(10)
	v_mfma_f32_32x32x16_bf16 v[96:111], v[96:99], v[124:127], 0
	v_add_f32_e32 v2, v70, v2
	v_add_f32_e32 v2, v71, v2
	v_add_f32_e32 v2, v72, v2
	v_add_f32_e32 v2, v73, v2
	v_cvt_pk_bf16_f32 v142, v68, v69
	v_cvt_pk_bf16_f32 v143, v70, v71
	ds_read_b64_tr_b16 v[144:145], v12 offset:25600
	ds_read_b64_tr_b16 v[146:147], v12 offset:26112
	s_waitcnt lgkmcnt(11)
	v_mfma_f32_32x32x16_bf16 v[80:95], v[148:151], v[120:123], v[80:95]
	v_add_f32_e32 v2, v74, v2
	v_add_f32_e32 v2, v75, v2
	v_add_f32_e32 v2, v76, v2
	v_add_f32_e32 v2, v77, v2
	v_cvt_pk_bf16_f32 v136, v72, v73
	v_cvt_pk_bf16_f32 v137, v74, v75
	ds_read_b64_tr_b16 v[148:149], v12 offset:29696
	ds_read_b64_tr_b16 v[150:151], v12 offset:30208
	s_waitcnt lgkmcnt(12)
	v_mfma_f32_32x32x16_bf16 v[96:111], v[176:179], v[120:123], v[96:111]
	v_add_f32_e32 v2, v78, v2
	v_add_f32_e32 v2, v79, v2
	v_add_f32_e32 v2, v48, v2
	v_add_f32_e32 v2, v49, v2
	v_cvt_pk_bf16_f32 v138, v76, v77
	v_cvt_pk_bf16_f32 v139, v78, v79
	ds_read_b64_tr_b16 v[176:177], v12 offset:26624
	ds_read_b64_tr_b16 v[178:179], v12 offset:27136
	s_waitcnt lgkmcnt(13)
	v_mfma_f32_32x32x16_bf16 v[80:95], v[172:175], v[116:119], v[80:95]
	v_add_f32_e32 v2, v50, v2
	v_add_f32_e32 v2, v51, v2
	v_add_f32_e32 v2, v52, v2
	v_add_f32_e32 v6, v53, v2
	v_cvt_pk_bf16_f32 v132, v48, v49
	v_cvt_pk_bf16_f32 v133, v50, v51
	ds_read_b64_tr_b16 v[2:3], v12 offset:30720
	ds_read_b64_tr_b16 v[4:5], v12 offset:31232
	s_waitcnt lgkmcnt(14)
	v_mfma_f32_32x32x16_bf16 v[96:111], v[164:167], v[116:119], v[96:111]
	v_add_f32_e32 v6, v54, v6
	v_add_f32_e32 v6, v55, v6
	v_add_f32_e32 v6, v56, v6
	v_add_f32_e32 v10, v57, v6
	v_cvt_pk_bf16_f32 v134, v52, v53
	v_cvt_pk_bf16_f32 v135, v54, v55
	ds_read_b64_tr_b16 v[6:7], v12 offset:27648
	ds_read_b64_tr_b16 v[8:9], v12 offset:28160
	s_waitcnt lgkmcnt(14)
	v_mfma_f32_32x32x16_bf16 v[80:95], v[168:171], v[112:115], v[80:95]
	v_add_f32_e32 v10, v58, v10
	v_add_f32_e32 v10, v59, v10
	v_add_f32_e32 v10, v60, v10
	v_add_f32_e32 v15, v61, v10
	v_cvt_pk_bf16_f32 v128, v56, v57
	v_cvt_pk_bf16_f32 v129, v58, v59
	ds_read_b64_tr_b16 v[10:11], v12 offset:31744
	ds_read_b64_tr_b16 v[12:13], v12 offset:32256
	v_mfma_f32_32x32x16_bf16 v[96:111], v[160:163], v[112:115], v[96:111]
	v_add_f32_e32 v15, v62, v15
	v_add_f32_e32 v15, v63, v15
	v_add_f32_e32 v15, 0, v15
	v_cvt_pk_bf16_f32 v130, v60, v61
	v_cvt_pk_bf16_f32 v131, v62, v63
	v_lshl_add_u64 v[48:49], v[186:187], 0, s[22:23]
	s_add_i32 s29, s57, s63
	s_mov_b32 s38, m0
	s_mov_b32 m0, s29
	s_nop 0
	global_load_lds_dwordx4 v[48:49], off
	s_mov_b32 m0, s38
	v_lshl_add_u64 v[48:49], v[188:189], 0, s[70:71]
	s_add_i32 s29, s65, s62
	s_mov_b32 s38, m0
	s_mov_b32 m0, s29
	s_nop 0
	global_load_lds_dwordx4 v[48:49], off
	s_mov_b32 m0, s38
	s_waitcnt vmcnt(7)
	v_mul_f32_e32 v48, v201, v191
	v_cmp_nge_f32_e32 vcc, s73, v48
	v_cmp_neq_f32_e64 s[38:39], 0, v207
	s_or_b64 vcc, vcc, s[38:39]
	v_cndmask_b32_e64 v48, 0, 1, vcc
	v_cmp_ne_u32_e64 s[38:39], 0, v48
	s_cmp_lg_u64 s[38:39], 0
	s_cselect_b64 s[38:39], -1, 0
	s_cbranch_vccz .LBB0_1084
	v_sub_f32_e32 v95, v95, v207
	v_sub_f32_e32 v94, v94, v207
	v_sub_f32_e32 v93, v93, v207
	v_sub_f32_e32 v92, v92, v207
	v_sub_f32_e32 v91, v91, v207
	v_sub_f32_e32 v90, v90, v207
	v_sub_f32_e32 v89, v89, v207
	v_sub_f32_e32 v88, v88, v207
	v_sub_f32_e32 v87, v87, v207
	v_sub_f32_e32 v86, v86, v207
	v_sub_f32_e32 v85, v85, v207
	v_sub_f32_e32 v84, v84, v207
	v_sub_f32_e32 v83, v83, v207
	v_sub_f32_e32 v82, v82, v207
	v_sub_f32_e32 v81, v81, v207
	v_sub_f32_e32 v80, v80, v207
	v_sub_f32_e32 v111, v111, v207
	v_sub_f32_e32 v110, v110, v207
	v_sub_f32_e32 v109, v109, v207
	v_sub_f32_e32 v108, v108, v207
	v_sub_f32_e32 v107, v107, v207
	v_sub_f32_e32 v106, v106, v207
	v_sub_f32_e32 v105, v105, v207
	v_sub_f32_e32 v104, v104, v207
	v_sub_f32_e32 v103, v103, v207
	v_sub_f32_e32 v102, v102, v207
	v_sub_f32_e32 v101, v101, v207
	v_sub_f32_e32 v100, v100, v207
	v_sub_f32_e32 v99, v99, v207
	v_sub_f32_e32 v98, v98, v207
	v_sub_f32_e32 v97, v97, v207
	v_sub_f32_e32 v96, v96, v207

.LBB0_1098:
	s_lshl_b64 s[52:53], s[80:81], 16
	s_lshl_b64 s[38:39], s[80:81], 2
	s_add_u32 s38, s34, s38
	s_addc_u32 s39, s35, s39
	v_lshl_add_u64 v[14:15], v[180:181], 2, s[38:39]
	s_add_i32 s80, s80, 4
	.p2align	6

.LBB0_1101:
	v_lshl_add_u64 v[222:223], v[218:219], 0, s[52:53]
	v_lshl_add_u64 v[50:51], v[222:223], 0, s[12:13]
	s_add_i32 s29, s56, s62
	s_mov_b32 s38, m0
	s_mov_b32 m0, s29
	s_nop 0
	global_load_lds_dwordx4 v[50:51], off
	s_mov_b32 m0, s38
	s_waitcnt vmcnt(7)
	v_mul_f32_e32 v49, v201, v209
	v_cmp_nge_f32_e32 vcc, s73, v49
	v_cmp_neq_f32_e64 s[38:39], 0, v207
	s_or_b64 vcc, vcc, s[38:39]
	v_cndmask_b32_e64 v49, 0, 1, vcc
	v_cmp_ne_u32_e64 s[38:39], 0, v49
	s_cmp_lg_u64 s[38:39], 0
	s_cselect_b64 s[38:39], -1, 0
	s_cbranch_vccz .LBB0_1103
	v_sub_f32_e32 v95, v95, v207
	v_sub_f32_e32 v94, v94, v207
	v_sub_f32_e32 v93, v93, v207
	v_sub_f32_e32 v92, v92, v207
	v_sub_f32_e32 v91, v91, v207
	v_sub_f32_e32 v90, v90, v207
	v_sub_f32_e32 v89, v89, v207
	v_sub_f32_e32 v88, v88, v207
	v_sub_f32_e32 v87, v87, v207
	v_sub_f32_e32 v86, v86, v207
	v_sub_f32_e32 v85, v85, v207
	v_sub_f32_e32 v84, v84, v207
	v_sub_f32_e32 v83, v83, v207
	v_sub_f32_e32 v82, v82, v207
	v_sub_f32_e32 v81, v81, v207
	v_sub_f32_e32 v80, v80, v207
	v_sub_f32_e32 v111, v111, v207
	v_sub_f32_e32 v110, v110, v207
	v_sub_f32_e32 v109, v109, v207
	v_sub_f32_e32 v108, v108, v207
	v_sub_f32_e32 v107, v107, v207
	v_sub_f32_e32 v106, v106, v207
	v_sub_f32_e32 v105, v105, v207
	v_sub_f32_e32 v104, v104, v207
	v_sub_f32_e32 v103, v103, v207
	v_sub_f32_e32 v102, v102, v207
	v_sub_f32_e32 v101, v101, v207
	v_sub_f32_e32 v100, v100, v207
	v_sub_f32_e32 v99, v99, v207
	v_sub_f32_e32 v98, v98, v207
	v_sub_f32_e32 v97, v97, v207
	v_sub_f32_e32 v96, v96, v207

.LBB0_1118:
	s_waitcnt vmcnt(7)
	v_mul_f32_e32 v49, v201, v226
	v_cmp_nge_f32_e32 vcc, s73, v49
	v_cmp_neq_f32_e64 s[40:41], 0, v207
	s_or_b64 vcc, vcc, s[40:41]
	v_cndmask_b32_e64 v49, 0, 1, vcc
	v_cmp_ne_u32_e64 s[40:41], 0, v49
	s_cmp_lg_u64 s[40:41], 0
	s_cselect_b64 s[40:41], -1, 0
	s_cbranch_vccz .LBB0_1120
	v_sub_f32_e32 v95, v95, v207
	v_sub_f32_e32 v94, v94, v207
	v_sub_f32_e32 v93, v93, v207
	v_sub_f32_e32 v92, v92, v207
	v_sub_f32_e32 v91, v91, v207
	v_sub_f32_e32 v90, v90, v207
	v_sub_f32_e32 v89, v89, v207
	v_sub_f32_e32 v88, v88, v207
	v_sub_f32_e32 v87, v87, v207
	v_sub_f32_e32 v86, v86, v207
	v_sub_f32_e32 v85, v85, v207
	v_sub_f32_e32 v84, v84, v207
	v_sub_f32_e32 v83, v83, v207
	v_sub_f32_e32 v82, v82, v207
	v_sub_f32_e32 v81, v81, v207
	v_sub_f32_e32 v80, v80, v207
	v_sub_f32_e32 v111, v111, v207
	v_sub_f32_e32 v110, v110, v207
	v_sub_f32_e32 v109, v109, v207
	v_sub_f32_e32 v108, v108, v207
	v_sub_f32_e32 v107, v107, v207
	v_sub_f32_e32 v106, v106, v207
	v_sub_f32_e32 v105, v105, v207
	v_sub_f32_e32 v104, v104, v207
	v_sub_f32_e32 v103, v103, v207
	v_sub_f32_e32 v102, v102, v207
	v_sub_f32_e32 v101, v101, v207
	v_sub_f32_e32 v100, v100, v207
	v_sub_f32_e32 v99, v99, v207
	v_sub_f32_e32 v98, v98, v207
	v_sub_f32_e32 v97, v97, v207
	v_sub_f32_e32 v96, v96, v207

.LBB0_1194:
	s_ashr_i32 s40, s62, 2
	s_ashr_i32 s41, s40, 31
	s_lshl_b64 s[40:41], s[40:41], 20
	s_add_u32 s17, s31, s40
	s_addc_u32 s41, s34, s41
	s_add_u32 s40, s17, s29
	s_addc_u32 s41, s41, 0
	s_and_b64 s[48:49], s[48:49], exec
	v_mov_b32_e32 v2, 0
	s_cselect_b32 s17, s41, s45
	s_cselect_b32 s29, s40, s44
	s_mov_b64 s[52:53], 0
	s_mov_b64 s[48:49], -1
	s_mov_b64 s[50:51], 0
	v_mov_b32_e32 v3, v2
	v_mov_b32_e32 v4, v2
	v_mov_b32_e32 v5, v2
	v_mov_b32_e32 v6, v2
	v_mov_b32_e32 v7, v2
	v_mov_b32_e32 v8, v2
	v_mov_b32_e32 v9, v2
	v_mov_b32_e32 v10, v2
	v_mov_b32_e32 v11, v2
	v_mov_b32_e32 v12, v2
	v_mov_b32_e32 v13, v2
	v_mov_b32_e32 v18, v2
	v_mov_b32_e32 v19, v2
	v_mov_b32_e32 v20, v2
	v_mov_b32_e32 v21, v2
	v_mov_b32_e32 v26, v2
	v_mov_b32_e32 v27, v2
	v_mov_b32_e32 v28, v2
	v_mov_b32_e32 v29, v2
	v_mov_b32_e32 v34, v2
	v_mov_b32_e32 v35, v2
	v_mov_b32_e32 v36, v2
	v_mov_b32_e32 v37, v2
	v_mov_b32_e32 v42, v2
	v_mov_b32_e32 v43, v2
	v_mov_b32_e32 v44, v2
	v_mov_b32_e32 v45, v2
	v_mov_b32_e32 v50, v2
	v_mov_b32_e32 v51, v2
	v_mov_b32_e32 v52, v2
	v_mov_b32_e32 v53, v2
	v_mov_b32_e32 v14, v2
	v_mov_b32_e32 v15, v2
	v_mov_b32_e32 v16, v2
	v_mov_b32_e32 v17, v2
	v_mov_b32_e32 v22, v2
	v_mov_b32_e32 v23, v2
	v_mov_b32_e32 v24, v2
	v_mov_b32_e32 v25, v2
	v_mov_b32_e32 v30, v2
	v_mov_b32_e32 v31, v2
	v_mov_b32_e32 v32, v2
	v_mov_b32_e32 v33, v2
	v_mov_b32_e32 v38, v2
	v_mov_b32_e32 v39, v2
	v_mov_b32_e32 v40, v2
	v_mov_b32_e32 v41, v2
	v_mov_b32_e32 v46, v2
	v_mov_b32_e32 v47, v2
	v_mov_b32_e32 v48, v2
	v_mov_b32_e32 v49, v2
	v_mov_b32_e32 v54, v2
	v_mov_b32_e32 v55, v2
	v_mov_b32_e32 v56, v2
	v_mov_b32_e32 v57, v2
	v_mov_b32_e32 v58, v2
	v_mov_b32_e32 v59, v2
	v_mov_b32_e32 v60, v2
	v_mov_b32_e32 v61, v2
	v_mov_b32_e32 v62, v2
	v_mov_b32_e32 v63, v2
	v_mov_b32_e32 v64, v2
	v_mov_b32_e32 v65, v2
	v_mov_b32_e32 v66, v2
	v_mov_b32_e32 v67, v2
	v_mov_b32_e32 v68, v2
	v_mov_b32_e32 v69, v2
	v_mov_b32_e32 v70, v2
	v_mov_b32_e32 v71, v2
	v_mov_b32_e32 v72, v2
	v_mov_b32_e32 v73, v2
	v_mov_b32_e32 v74, v2
	v_mov_b32_e32 v75, v2
	v_mov_b32_e32 v76, v2
	v_mov_b32_e32 v77, v2
	v_mov_b32_e32 v82, v2
	v_mov_b32_e32 v83, v2
	v_mov_b32_e32 v84, v2
	v_mov_b32_e32 v85, v2
	v_mov_b32_e32 v90, v2
	v_mov_b32_e32 v91, v2
	v_mov_b32_e32 v92, v2
	v_mov_b32_e32 v93, v2
	v_mov_b32_e32 v98, v2
	v_mov_b32_e32 v99, v2
	v_mov_b32_e32 v100, v2
	v_mov_b32_e32 v101, v2
	v_mov_b32_e32 v106, v2
	v_mov_b32_e32 v107, v2
	v_mov_b32_e32 v108, v2
	v_mov_b32_e32 v109, v2
	v_mov_b32_e32 v114, v2
	v_mov_b32_e32 v115, v2
	v_mov_b32_e32 v116, v2
	v_mov_b32_e32 v117, v2
	v_mov_b32_e32 v78, v2
	v_mov_b32_e32 v79, v2
	v_mov_b32_e32 v80, v2
	v_mov_b32_e32 v81, v2
	v_mov_b32_e32 v86, v2
	v_mov_b32_e32 v87, v2
	v_mov_b32_e32 v88, v2
	v_mov_b32_e32 v89, v2
	v_mov_b32_e32 v94, v2
	v_mov_b32_e32 v95, v2
	v_mov_b32_e32 v96, v2
	v_mov_b32_e32 v97, v2
	v_mov_b32_e32 v102, v2
	v_mov_b32_e32 v103, v2
	v_mov_b32_e32 v104, v2
	v_mov_b32_e32 v105, v2
	v_mov_b32_e32 v110, v2
	v_mov_b32_e32 v111, v2
	v_mov_b32_e32 v112, v2
	v_mov_b32_e32 v113, v2
	v_mov_b32_e32 v118, v2
	v_mov_b32_e32 v119, v2
	v_mov_b32_e32 v120, v2
	v_mov_b32_e32 v121, v2
	v_mov_b32_e32 v122, v2
	v_mov_b32_e32 v123, v2
	v_mov_b32_e32 v124, v2
	v_mov_b32_e32 v125, v2
	v_mov_b32_e32 v126, v2
	v_mov_b32_e32 v127, v2
	v_mov_b32_e32 v128, v2
	v_mov_b32_e32 v129, v2
	.p2align	6

.LBB0_1212:
	s_ashr_i32 s44, s62, 2
	s_ashr_i32 s45, s44, 31
	s_lshl_b64 s[44:45], s[44:45], 20
	s_add_u32 s37, s31, s44
	s_addc_u32 s44, s34, s45
	s_add_u32 s29, s37, s29
	s_addc_u32 s37, s44, s81
	s_add_u32 s44, s29, 0x800
	s_addc_u32 s45, s37, 0
	s_and_b64 s[48:49], s[16:17], exec
	v_mov_b32_e32 v2, 0
	s_cselect_b32 s37, s45, s39
	s_cselect_b32 s29, s44, s38
	s_mov_b64 s[52:53], 0
	s_mov_b64 s[48:49], -1
	s_mov_b64 s[50:51], 0
	v_mov_b32_e32 v3, v2
	v_mov_b32_e32 v4, v2
	v_mov_b32_e32 v5, v2
	v_mov_b32_e32 v6, v2
	v_mov_b32_e32 v7, v2
	v_mov_b32_e32 v8, v2
	v_mov_b32_e32 v9, v2
	v_mov_b32_e32 v10, v2
	v_mov_b32_e32 v11, v2
	v_mov_b32_e32 v12, v2
	v_mov_b32_e32 v13, v2
	v_mov_b32_e32 v14, v2
	v_mov_b32_e32 v15, v2
	v_mov_b32_e32 v16, v2
	v_mov_b32_e32 v17, v2
	v_mov_b32_e32 v26, v2
	v_mov_b32_e32 v27, v2
	v_mov_b32_e32 v28, v2
	v_mov_b32_e32 v29, v2
	v_mov_b32_e32 v30, v2
	v_mov_b32_e32 v31, v2
	v_mov_b32_e32 v32, v2
	v_mov_b32_e32 v33, v2
	v_mov_b32_e32 v42, v2
	v_mov_b32_e32 v43, v2
	v_mov_b32_e32 v44, v2
	v_mov_b32_e32 v45, v2
	v_mov_b32_e32 v46, v2
	v_mov_b32_e32 v47, v2
	v_mov_b32_e32 v48, v2
	v_mov_b32_e32 v49, v2
	v_mov_b32_e32 v18, v2
	v_mov_b32_e32 v19, v2
	v_mov_b32_e32 v20, v2
	v_mov_b32_e32 v21, v2
	v_mov_b32_e32 v22, v2
	v_mov_b32_e32 v23, v2
	v_mov_b32_e32 v24, v2
	v_mov_b32_e32 v25, v2
	v_mov_b32_e32 v34, v2
	v_mov_b32_e32 v35, v2
	v_mov_b32_e32 v36, v2
	v_mov_b32_e32 v37, v2
	v_mov_b32_e32 v38, v2
	v_mov_b32_e32 v39, v2
	v_mov_b32_e32 v40, v2
	v_mov_b32_e32 v41, v2
	v_mov_b32_e32 v50, v2
	v_mov_b32_e32 v51, v2
	v_mov_b32_e32 v52, v2
	v_mov_b32_e32 v53, v2
	v_mov_b32_e32 v54, v2
	v_mov_b32_e32 v55, v2
	v_mov_b32_e32 v56, v2
	v_mov_b32_e32 v57, v2
	v_mov_b32_e32 v58, v2
	v_mov_b32_e32 v59, v2
	v_mov_b32_e32 v60, v2
	v_mov_b32_e32 v61, v2
	v_mov_b32_e32 v62, v2
	v_mov_b32_e32 v63, v2
	v_mov_b32_e32 v64, v2
	v_mov_b32_e32 v65, v2
	v_mov_b32_e32 v66, v2
	v_mov_b32_e32 v67, v2
	v_mov_b32_e32 v68, v2
	v_mov_b32_e32 v69, v2
	v_mov_b32_e32 v70, v2
	v_mov_b32_e32 v71, v2
	v_mov_b32_e32 v72, v2
	v_mov_b32_e32 v73, v2
	v_mov_b32_e32 v74, v2
	v_mov_b32_e32 v75, v2
	v_mov_b32_e32 v76, v2
	v_mov_b32_e32 v77, v2
	v_mov_b32_e32 v78, v2
	v_mov_b32_e32 v79, v2
	v_mov_b32_e32 v80, v2
	v_mov_b32_e32 v81, v2
	v_mov_b32_e32 v90, v2
	v_mov_b32_e32 v91, v2
	v_mov_b32_e32 v92, v2
	v_mov_b32_e32 v93, v2
	v_mov_b32_e32 v94, v2
	v_mov_b32_e32 v95, v2
	v_mov_b32_e32 v96, v2
	v_mov_b32_e32 v97, v2
	v_mov_b32_e32 v106, v2
	v_mov_b32_e32 v107, v2
	v_mov_b32_e32 v108, v2
	v_mov_b32_e32 v109, v2
	v_mov_b32_e32 v110, v2
	v_mov_b32_e32 v111, v2
	v_mov_b32_e32 v112, v2
	v_mov_b32_e32 v113, v2
	v_mov_b32_e32 v82, v2
	v_mov_b32_e32 v83, v2
	v_mov_b32_e32 v84, v2
	v_mov_b32_e32 v85, v2
	v_mov_b32_e32 v86, v2
	v_mov_b32_e32 v87, v2
	v_mov_b32_e32 v88, v2
	v_mov_b32_e32 v89, v2
	v_mov_b32_e32 v98, v2
	v_mov_b32_e32 v99, v2
	v_mov_b32_e32 v100, v2
	v_mov_b32_e32 v101, v2
	v_mov_b32_e32 v102, v2
	v_mov_b32_e32 v103, v2
	v_mov_b32_e32 v104, v2
	v_mov_b32_e32 v105, v2
	v_mov_b32_e32 v114, v2
	v_mov_b32_e32 v115, v2
	v_mov_b32_e32 v116, v2
	v_mov_b32_e32 v117, v2
	v_mov_b32_e32 v118, v2
	v_mov_b32_e32 v119, v2
	v_mov_b32_e32 v120, v2
	v_mov_b32_e32 v121, v2
	v_mov_b32_e32 v122, v2
	v_mov_b32_e32 v123, v2
	v_mov_b32_e32 v124, v2
	v_mov_b32_e32 v125, v2
	v_mov_b32_e32 v126, v2
	v_mov_b32_e32 v127, v2
	v_mov_b32_e32 v128, v2
	v_mov_b32_e32 v129, v2
	.p2align	6

.LBB0_1237:
	s_add_i32 s29, s29, 24
	s_add_i32 s40, s40, 8
	v_add_u32_e32 v111, 0xc00, v111
	s_cmp_gt_i32 s40, s1
	v_add_u32_e32 v110, 0x300, v110
	s_cbranch_scc1 .LBB0_1248
	.p2align	6

.LBB0_2005:
	s_ashr_i32 s47, s46, 31
	s_lshl_b64 s[52:53], s[46:47], 19
	v_readlane_b32 s40, v253, 34
	v_readlane_b32 s41, v253, 35
	s_add_u32 s52, s40, s52
	s_addc_u32 s53, s41, s53
	s_and_b64 s[56:57], s[54:55], exec
	s_cselect_b32 s29, s53, s37
	s_cselect_b32 s47, s52, s36
	s_ashr_i32 s49, s48, 31
	s_lshl_b64 s[56:57], s[48:49], 19
	s_add_u32 s56, s35, s56
	s_addc_u32 s57, s64, s57
	s_and_b64 s[62:63], s[54:55], exec
	s_cselect_b32 s49, s57, s61
	s_cselect_b32 s59, s56, s60
	s_add_u32 s36, s36, 0x40080
	s_addc_u32 s37, s37, 0
	s_add_u32 s80, s60, 0x100
	v_mov_b32_e32 v2, 0
	s_addc_u32 s95, s61, 0
	s_mov_b32 vcc_lo, -2
	v_mov_b32_e32 v3, v2
	v_mov_b32_e32 v4, v2
	v_mov_b32_e32 v5, v2
	v_mov_b32_e32 v6, v2
	v_mov_b32_e32 v7, v2
	v_mov_b32_e32 v8, v2
	v_mov_b32_e32 v9, v2
	v_mov_b32_e32 v10, v2
	v_mov_b32_e32 v11, v2
	v_mov_b32_e32 v12, v2
	v_mov_b32_e32 v13, v2
	v_mov_b32_e32 v18, v2
	v_mov_b32_e32 v19, v2
	v_mov_b32_e32 v20, v2
	v_mov_b32_e32 v21, v2
	v_mov_b32_e32 v26, v2
	v_mov_b32_e32 v27, v2
	v_mov_b32_e32 v28, v2
	v_mov_b32_e32 v29, v2
	v_mov_b32_e32 v34, v2
	v_mov_b32_e32 v35, v2
	v_mov_b32_e32 v36, v2
	v_mov_b32_e32 v37, v2
	v_mov_b32_e32 v42, v2
	v_mov_b32_e32 v43, v2
	v_mov_b32_e32 v44, v2
	v_mov_b32_e32 v45, v2
	v_mov_b32_e32 v50, v2
	v_mov_b32_e32 v51, v2
	v_mov_b32_e32 v52, v2
	v_mov_b32_e32 v53, v2
	v_mov_b32_e32 v14, v2
	v_mov_b32_e32 v15, v2
	v_mov_b32_e32 v16, v2
	v_mov_b32_e32 v17, v2
	v_mov_b32_e32 v22, v2
	v_mov_b32_e32 v23, v2
	v_mov_b32_e32 v24, v2
	v_mov_b32_e32 v25, v2
	v_mov_b32_e32 v30, v2
	v_mov_b32_e32 v31, v2
	v_mov_b32_e32 v32, v2
	v_mov_b32_e32 v33, v2
	v_mov_b32_e32 v38, v2
	v_mov_b32_e32 v39, v2
	v_mov_b32_e32 v40, v2
	v_mov_b32_e32 v41, v2
	v_mov_b32_e32 v46, v2
	v_mov_b32_e32 v47, v2
	v_mov_b32_e32 v48, v2
	v_mov_b32_e32 v49, v2
	v_mov_b32_e32 v54, v2
	v_mov_b32_e32 v55, v2
	v_mov_b32_e32 v56, v2
	v_mov_b32_e32 v57, v2
	v_mov_b32_e32 v58, v2
	v_mov_b32_e32 v59, v2
	v_mov_b32_e32 v60, v2
	v_mov_b32_e32 v61, v2
	v_mov_b32_e32 v62, v2
	v_mov_b32_e32 v63, v2
	v_mov_b32_e32 v64, v2
	v_mov_b32_e32 v65, v2
	v_mov_b32_e32 v66, v2
	v_mov_b32_e32 v67, v2
	v_mov_b32_e32 v68, v2
	v_mov_b32_e32 v69, v2
	v_mov_b32_e32 v70, v2
	v_mov_b32_e32 v71, v2
	v_mov_b32_e32 v72, v2
	v_mov_b32_e32 v73, v2
	v_mov_b32_e32 v78, v2
	v_mov_b32_e32 v79, v2
	v_mov_b32_e32 v80, v2
	v_mov_b32_e32 v81, v2
	v_mov_b32_e32 v86, v2
	v_mov_b32_e32 v87, v2
	v_mov_b32_e32 v88, v2
	v_mov_b32_e32 v89, v2
	v_mov_b32_e32 v94, v2
	v_mov_b32_e32 v95, v2
	v_mov_b32_e32 v96, v2
	v_mov_b32_e32 v97, v2
	v_mov_b32_e32 v102, v2
	v_mov_b32_e32 v103, v2
	v_mov_b32_e32 v104, v2
	v_mov_b32_e32 v105, v2
	v_mov_b32_e32 v110, v2
	v_mov_b32_e32 v111, v2
	v_mov_b32_e32 v112, v2
	v_mov_b32_e32 v113, v2
	v_mov_b32_e32 v118, v2
	v_mov_b32_e32 v119, v2
	v_mov_b32_e32 v120, v2
	v_mov_b32_e32 v121, v2
	v_mov_b32_e32 v74, v2
	v_mov_b32_e32 v75, v2
	v_mov_b32_e32 v76, v2
	v_mov_b32_e32 v77, v2
	v_mov_b32_e32 v82, v2
	v_mov_b32_e32 v83, v2
	v_mov_b32_e32 v84, v2
	v_mov_b32_e32 v85, v2
	v_mov_b32_e32 v90, v2
	v_mov_b32_e32 v91, v2
	v_mov_b32_e32 v92, v2
	v_mov_b32_e32 v93, v2
	v_mov_b32_e32 v98, v2
	v_mov_b32_e32 v99, v2
	v_mov_b32_e32 v100, v2
	v_mov_b32_e32 v101, v2
	v_mov_b32_e32 v106, v2
	v_mov_b32_e32 v107, v2
	v_mov_b32_e32 v108, v2
	v_mov_b32_e32 v109, v2
	v_mov_b32_e32 v114, v2
	v_mov_b32_e32 v115, v2
	v_mov_b32_e32 v116, v2
	v_mov_b32_e32 v117, v2
	v_mov_b32_e32 v122, v2
	v_mov_b32_e32 v123, v2
	v_mov_b32_e32 v124, v2
	v_mov_b32_e32 v125, v2
	v_mov_b32_e32 v126, v2
	v_mov_b32_e32 v127, v2
	v_mov_b32_e32 v128, v2
	v_mov_b32_e32 v129, v2
	.p2align	6

.LBB0_2066:
	s_add_u32 s52, s52, 0x40080
	s_addc_u32 s53, s53, 0
	s_add_u32 s17, s54, 0x100
	v_mov_b32_e32 v2, 0
	s_addc_u32 s29, s55, 0
	s_mov_b32 s39, -2
	v_mov_b32_e32 v3, v2
	v_mov_b32_e32 v4, v2
	v_mov_b32_e32 v5, v2
	v_mov_b32_e32 v6, v2
	v_mov_b32_e32 v7, v2
	v_mov_b32_e32 v8, v2
	v_mov_b32_e32 v9, v2
	v_mov_b32_e32 v10, v2
	v_mov_b32_e32 v11, v2
	v_mov_b32_e32 v12, v2
	v_mov_b32_e32 v13, v2
	v_mov_b32_e32 v14, v2
	v_mov_b32_e32 v15, v2
	v_mov_b32_e32 v16, v2
	v_mov_b32_e32 v17, v2
	v_mov_b32_e32 v26, v2
	v_mov_b32_e32 v27, v2
	v_mov_b32_e32 v28, v2
	v_mov_b32_e32 v29, v2
	v_mov_b32_e32 v30, v2
	v_mov_b32_e32 v31, v2
	v_mov_b32_e32 v32, v2
	v_mov_b32_e32 v33, v2
	v_mov_b32_e32 v42, v2
	v_mov_b32_e32 v43, v2
	v_mov_b32_e32 v44, v2
	v_mov_b32_e32 v45, v2
	v_mov_b32_e32 v46, v2
	v_mov_b32_e32 v47, v2
	v_mov_b32_e32 v48, v2
	v_mov_b32_e32 v49, v2
	v_mov_b32_e32 v18, v2
	v_mov_b32_e32 v19, v2
	v_mov_b32_e32 v20, v2
	v_mov_b32_e32 v21, v2
	v_mov_b32_e32 v22, v2
	v_mov_b32_e32 v23, v2
	v_mov_b32_e32 v24, v2
	v_mov_b32_e32 v25, v2
	v_mov_b32_e32 v34, v2
	v_mov_b32_e32 v35, v2
	v_mov_b32_e32 v36, v2
	v_mov_b32_e32 v37, v2
	v_mov_b32_e32 v38, v2
	v_mov_b32_e32 v39, v2
	v_mov_b32_e32 v40, v2
	v_mov_b32_e32 v41, v2
	v_mov_b32_e32 v50, v2
	v_mov_b32_e32 v51, v2
	v_mov_b32_e32 v52, v2
	v_mov_b32_e32 v53, v2
	v_mov_b32_e32 v54, v2
	v_mov_b32_e32 v55, v2
	v_mov_b32_e32 v56, v2
	v_mov_b32_e32 v57, v2
	v_mov_b32_e32 v58, v2
	v_mov_b32_e32 v59, v2
	v_mov_b32_e32 v60, v2
	v_mov_b32_e32 v61, v2
	v_mov_b32_e32 v62, v2
	v_mov_b32_e32 v63, v2
	v_mov_b32_e32 v64, v2
	v_mov_b32_e32 v65, v2
	v_mov_b32_e32 v66, v2
	v_mov_b32_e32 v67, v2
	v_mov_b32_e32 v68, v2
	v_mov_b32_e32 v69, v2
	v_mov_b32_e32 v70, v2
	v_mov_b32_e32 v71, v2
	v_mov_b32_e32 v72, v2
	v_mov_b32_e32 v73, v2
	v_mov_b32_e32 v74, v2
	v_mov_b32_e32 v75, v2
	v_mov_b32_e32 v76, v2
	v_mov_b32_e32 v77, v2
	v_mov_b32_e32 v78, v2
	v_mov_b32_e32 v79, v2
	v_mov_b32_e32 v80, v2
	v_mov_b32_e32 v81, v2
	v_mov_b32_e32 v90, v2
	v_mov_b32_e32 v91, v2
	v_mov_b32_e32 v92, v2
	v_mov_b32_e32 v93, v2
	v_mov_b32_e32 v94, v2
	v_mov_b32_e32 v95, v2
	v_mov_b32_e32 v96, v2
	v_mov_b32_e32 v97, v2
	v_mov_b32_e32 v106, v2
	v_mov_b32_e32 v107, v2
	v_mov_b32_e32 v108, v2
	v_mov_b32_e32 v109, v2
	v_mov_b32_e32 v110, v2
	v_mov_b32_e32 v111, v2
	v_mov_b32_e32 v112, v2
	v_mov_b32_e32 v113, v2
	v_mov_b32_e32 v82, v2
	v_mov_b32_e32 v83, v2
	v_mov_b32_e32 v84, v2
	v_mov_b32_e32 v85, v2
	v_mov_b32_e32 v86, v2
	v_mov_b32_e32 v87, v2
	v_mov_b32_e32 v88, v2
	v_mov_b32_e32 v89, v2
	v_mov_b32_e32 v98, v2
	v_mov_b32_e32 v99, v2
	v_mov_b32_e32 v100, v2
	v_mov_b32_e32 v101, v2
	v_mov_b32_e32 v102, v2
	v_mov_b32_e32 v103, v2
	v_mov_b32_e32 v104, v2
	v_mov_b32_e32 v105, v2
	v_mov_b32_e32 v114, v2
	v_mov_b32_e32 v115, v2
	v_mov_b32_e32 v116, v2
	v_mov_b32_e32 v117, v2
	v_mov_b32_e32 v118, v2
	v_mov_b32_e32 v119, v2
	v_mov_b32_e32 v120, v2
	v_mov_b32_e32 v121, v2
	v_mov_b32_e32 v122, v2
	v_mov_b32_e32 v123, v2
	v_mov_b32_e32 v124, v2
	v_mov_b32_e32 v125, v2
	v_mov_b32_e32 v126, v2
	v_mov_b32_e32 v127, v2
	v_mov_b32_e32 v128, v2
	v_mov_b32_e32 v129, v2
	.p2align	6
